# baseline (speedup 1.0000x reference)
.LBB1_151:
	s_or_b64 exec, exec, s[12:13]
	s_waitcnt vmcnt(0) lgkmcnt(0)
	v_mov_b32_dpp v2, v26 quad_perm:[0,0,0,0] row_mask:0xf bank_mask:0xf bound_ctrl:1
	v_lshl_or_b32 v3, v2, 7, v56
	v_cmp_lt_i32_e32 vcc, -1, v2
	v_mov_b32_dpp v10, v26 quad_perm:[1,1,1,1] row_mask:0xf bank_mask:0xf bound_ctrl:1
	v_lshl_or_b32 v11, v10, 7, v56
	v_cndmask_b32_e32 v2, v58, v3, vcc
	v_cmp_lt_i32_e32 vcc, -1, v10
	v_mov_b32_dpp v14, v26 quad_perm:[2,2,2,2] row_mask:0xf bank_mask:0xf bound_ctrl:1
	v_lshl_or_b32 v15, v14, 7, v56
	v_cndmask_b32_e32 v10, v58, v11, vcc
	v_cmp_lt_i32_e32 vcc, -1, v14
	v_mov_b32_dpp v26, v26 quad_perm:[3,3,3,3] row_mask:0xf bank_mask:0xf bound_ctrl:1
	v_lshl_or_b32 v27, v26, 7, v56
	v_cndmask_b32_e32 v14, v58, v15, vcc
	v_cmp_lt_i32_e32 vcc, -1, v26
	buffer_load_dwordx4 v[6:9], v2, s[4:7], 0 offen nt
	s_nop 0
	buffer_load_dwordx4 v[2:5], v2, s[4:7], 0 offen offset:64 nt
	v_cndmask_b32_e32 v26, v58, v27, vcc
	buffer_load_dwordx4 v[18:21], v10, s[4:7], 0 offen nt
	s_nop 0
	buffer_load_dwordx4 v[10:13], v10, s[4:7], 0 offen offset:64 nt
	s_nop 0
	buffer_load_dwordx4 v[22:25], v14, s[4:7], 0 offen nt
	s_nop 0
	buffer_load_dwordx4 v[14:17], v14, s[4:7], 0 offen offset:64 nt
	s_nop 0
	buffer_load_dwordx4 v[30:33], v26, s[4:7], 0 offen nt
	s_nop 0
	buffer_load_dwordx4 v[26:29], v26, s[4:7], 0 offen offset:64 nt
	s_waitcnt vmcnt(5)
	v_pk_add_f16 v6, v6, v18
	s_waitcnt vmcnt(4)
	v_pk_add_f16 v2, v2, v10
	s_waitcnt vmcnt(1)
	v_pk_add_f16 v18, v22, v30
	s_waitcnt vmcnt(0)
	v_pk_add_f16 v10, v14, v26
	v_pk_add_f16 v3, v3, v11
	s_add_i32 s17, s17, 4
	v_pk_add_f16 v6, v6, v18
	v_pk_add_f16 v2, v2, v10
	v_cmp_ge_i32_e32 vcc, s17, v1
	v_fma_mix_f32 v53, v6, 1.0, v53 op_sel:[0,0,0] op_sel_hi:[1,0,0]
	v_fma_mix_f32 v44, v6, 1.0, v44 op_sel:[1,0,0] op_sel_hi:[1,0,0]
	v_fma_mix_f32 v54, v2, 1.0, v54 op_sel:[0,0,0] op_sel_hi:[1,0,0]
	v_fma_mix_f32 v42, v2, 1.0, v42 op_sel:[1,0,0] op_sel_hi:[1,0,0]
	v_pk_add_f16 v2, v7, v19
	v_pk_add_f16 v6, v23, v31
	s_or_b64 s[10:11], vcc, s[10:11]
	v_pk_add_f16 v2, v2, v6
	v_pk_add_f16 v6, v15, v27
	v_add_u32_e32 v46, 16, v46
	v_pk_add_f16 v3, v3, v6
	v_fma_mix_f32 v45, v2, 1.0, v45 op_sel:[0,0,0] op_sel_hi:[1,0,0]
	v_fma_mix_f32 v40, v2, 1.0, v40 op_sel:[1,0,0] op_sel_hi:[1,0,0]
	v_pk_add_f16 v2, v8, v20
	s_nop 0
	v_fma_mix_f32 v43, v3, 1.0, v43 op_sel:[0,0,0] op_sel_hi:[1,0,0]
	v_fma_mix_f32 v38, v3, 1.0, v38 op_sel:[1,0,0] op_sel_hi:[1,0,0]
	v_pk_add_f16 v3, v24, v32
	s_nop 0
	v_pk_add_f16 v2, v2, v3
	v_pk_add_f16 v3, v4, v12
	v_pk_add_f16 v4, v16, v28
	s_nop 0
	v_pk_add_f16 v3, v3, v4
	v_fma_mix_f32 v41, v2, 1.0, v41 op_sel:[0,0,0] op_sel_hi:[1,0,0]
	v_fma_mix_f32 v36, v2, 1.0, v36 op_sel:[1,0,0] op_sel_hi:[1,0,0]
	v_pk_add_f16 v2, v9, v21
	v_pk_add_f16 v4, v17, v29
	s_nop 0
	v_fma_mix_f32 v39, v3, 1.0, v39 op_sel:[0,0,0] op_sel_hi:[1,0,0]
	v_fma_mix_f32 v34, v3, 1.0, v34 op_sel:[1,0,0] op_sel_hi:[1,0,0]
	v_pk_add_f16 v3, v25, v33
	s_nop 0
	v_pk_add_f16 v2, v2, v3
	v_pk_add_f16 v3, v5, v13
	s_nop 0
	v_pk_add_f16 v3, v3, v4
	v_fma_mix_f32 v37, v2, 1.0, v37 op_sel:[0,0,0] op_sel_hi:[1,0,0]
	v_fma_mix_f32 v52, v2, 1.0, v52 op_sel:[1,0,0] op_sel_hi:[1,0,0]
	s_nop 0
	v_fma_mix_f32 v35, v3, 1.0, v35 op_sel:[0,0,0] op_sel_hi:[1,0,0]
	v_fma_mix_f32 v50, v3, 1.0, v50 op_sel:[1,0,0] op_sel_hi:[1,0,0]
	s_andn2_b64 exec, exec, s[10:11]
	s_cbranch_execz .LBB1_157
